# k1: step-0 zero-state stores of the 64 state chains (critical path) moved to the paired workgroup bid+64, which has slack
# baseline (speedup 1.0000x reference)
.LBB0_714:
	s_lshl_b32 s52, s49, 8
	s_ashr_i32 s53, s52, 31
	s_cmp_eq_u32 s49, 0
	s_mov_b32 s8, 0xfff00000
	s_cselect_b32 s37, -1, 0
	s_cselect_b32 s36, s8, 0x100000
	s_ashr_i32 s49, s48, 31
	v_lshl_add_u64 v[68:69], s[48:49], 0, v[210:211]
	v_lshlrev_b64 v[68:69], 11, v[68:69]
	v_lshl_add_u64 v[68:69], s[34:35], 0, v[68:69]
	v_lshl_add_u64 v[68:69], s[52:53], 1, v[68:69]
	v_lshlrev_b32_e32 v66, 1, v216
	s_cmp_eq_u32 s74, -1
	v_lshl_add_u64 v[68:69], v[68:69], 0, v[66:67]
	v_cvt_pk_bf16_f32 v134, v130, v131
	v_cvt_pk_bf16_f32 v135, v132, v133
	v_cvt_pk_bf16_f32 v136, v126, v127
	v_cvt_pk_bf16_f32 v137, v128, v129
	s_cselect_b64 s[54:55], -1, 0
	s_cmp_lg_u32 s74, -1
	v_mov_b32_e32 v236, v213
	global_store_dwordx4 v[68:69], v[134:137], off offset:1024
	s_nop 1
	v_cvt_pk_bf16_f32 v134, v98, v99
	v_cvt_pk_bf16_f32 v135, v100, v101
	v_cvt_pk_bf16_f32 v136, v94, v95
	v_cvt_pk_bf16_f32 v137, v96, v97
	global_store_dwordx4 v[68:69], v[134:137], off offset:1280
	s_cbranch_scc1 .LBB0_716
	s_mov_b32 s74, s73
	s_mov_b32 s75, s73
	s_mov_b32 s72, s73
	v_mov_b64_e32 v[136:137], s[74:75]
	v_lshl_add_u64 v[68:69], v[68:69], 0, s[36:37]
	v_mov_b64_e32 v[134:135], s[72:73]
	global_store_dwordx4 v[68:69], v[134:137], off offset:1024
	global_store_dwordx4 v[68:69], v[134:137], off offset:1280

.LBB0_746:
	s_waitcnt vmcnt(0)
	v_readlane_b32 s88, v254, 61
	v_readlane_b32 s50, v255, 0
	s_barrier
	v_readlane_b32 s87, v254, 60
	v_readlane_b32 s89, v254, 62
	v_readlane_b32 s51, v255, 1
	s_sub_i32 s4, s2, 64
	s_lshr_b32 s5, s4, 2
	s_bfe_u32 s6, s4, 0x10001
	s_and_b32 s7, s4, 1
	s_lshl_b32 s5, s5, 3
	s_mul_i32 s10, s6, 7
	s_add_i32 s5, s5, s10
	s_lshl_b32 s5, s5, 20
	s_lshl_b32 s7, s7, 19
	s_add_i32 s5, s5, s7
	s_lshl_b32 s6, s6, 9
	s_add_i32 s5, s5, s6
	s_addk_i32 s5, 0x400
	s_load_dwordx2 s[8:9], s[88:89], 0x88
	v_lshrrev_b32_e32 v2, 5, v0
	v_lshlrev_b32_e32 v2, 11, v2
	v_and_b32_e32 v3, 31, v0
	v_lshl_or_b32 v2, v3, 4, v2
	v_mov_b32_e32 v3, 0
	v_mov_b32_e32 v4, 0
	v_mov_b32_e32 v5, 0
	v_mov_b32_e32 v6, 0
	v_mov_b32_e32 v7, 0
	s_waitcnt lgkmcnt(0)
	s_add_u32 s8, s8, 0x16a00000
	s_addc_u32 s9, s9, 0
	s_add_u32 s8, s8, s5
	s_addc_u32 s9, s9, 0
	v_lshl_add_u64 v[2:3], v[2:3], 0, s[8:9]
	s_mov_b32 s10, 0x8000
	s_mov_b32 s11, 0
	global_store_dwordx4 v[2:3], v[4:7], off
	v_lshl_add_u64 v[2:3], v[2:3], 0, s[10:11]
	global_store_dwordx4 v[2:3], v[4:7], off
	v_lshl_add_u64 v[2:3], v[2:3], 0, s[10:11]
	global_store_dwordx4 v[2:3], v[4:7], off
	v_lshl_add_u64 v[2:3], v[2:3], 0, s[10:11]
	global_store_dwordx4 v[2:3], v[4:7], off
	v_lshl_add_u64 v[2:3], v[2:3], 0, s[10:11]
	global_store_dwordx4 v[2:3], v[4:7], off
	v_lshl_add_u64 v[2:3], v[2:3], 0, s[10:11]
	global_store_dwordx4 v[2:3], v[4:7], off
	v_lshl_add_u64 v[2:3], v[2:3], 0, s[10:11]
	global_store_dwordx4 v[2:3], v[4:7], off
	v_lshl_add_u64 v[2:3], v[2:3], 0, s[10:11]
	global_store_dwordx4 v[2:3], v[4:7], off
	v_lshl_add_u64 v[2:3], v[2:3], 0, s[10:11]
	global_store_dwordx4 v[2:3], v[4:7], off
	v_lshl_add_u64 v[2:3], v[2:3], 0, s[10:11]
	global_store_dwordx4 v[2:3], v[4:7], off
	v_lshl_add_u64 v[2:3], v[2:3], 0, s[10:11]
	global_store_dwordx4 v[2:3], v[4:7], off
	v_lshl_add_u64 v[2:3], v[2:3], 0, s[10:11]
	global_store_dwordx4 v[2:3], v[4:7], off
	v_lshl_add_u64 v[2:3], v[2:3], 0, s[10:11]
	global_store_dwordx4 v[2:3], v[4:7], off
	v_lshl_add_u64 v[2:3], v[2:3], 0, s[10:11]
	global_store_dwordx4 v[2:3], v[4:7], off
	v_lshl_add_u64 v[2:3], v[2:3], 0, s[10:11]
	global_store_dwordx4 v[2:3], v[4:7], off
	v_lshl_add_u64 v[2:3], v[2:3], 0, s[10:11]
	global_store_dwordx4 v[2:3], v[4:7], off
	s_cbranch_execz .LBB0_694
	s_branch .LBB0_734
